# final combine phases: wave sum of squares via 4 DPP row-rotate adds + permlane16/32 swap adds instead of 6 serialized ds_bpermute round trips
# speedup vs baseline: 1.0024x; 1.0024x over previous
; __device__ __forceinline__ float bflo(unsigned w) { return __uint_as_float(w << 16); }
; __device__ __forceinline__ float bfhi(unsigned w) { return __uint_as_float(w & 0xffff0000u); }
; __device__ __forceinline__ void p_final(const Args& a, const Frame& F, int half) {
;     ...
;     for (int t = tbeg + gw; t < tend; t += NGW) {
;         f32x4* xr = (f32x4*)(a.out + (size_t)t * D) + F.lane;
;         const u32x2* x1p = (const u32x2*)x1_row(a.out, a.ws, t) + F.lane;
;         const f32x4* g2 = (const f32x4*)(mod + (t >> 13) * 6144 + 5120) + F.lane;
;         int rk[4]; float wk[4];
; #pragma unroll
;         for (int k = 0; k < 4; ++k) { rk[k] = rkn[k]; wk[k] = wkn[k]; }
;         u32x2 ok[4][4], xw[4];
; #pragma unroll
;         for (int j = 0; j < 4; ++j) { xw[j] = x1p[64 * j];
; #pragma unroll
;             for (int k = 0; k < 4; ++k) ok[j][k] = *((const u32x2*)(OUTK + (size_t)rk[k] * D) + F.lane + 64 * j); }
;         { const int tn = t + NGW; if (tn < tend) {
; #pragma unroll
;             for (int k = 0; k < 4; ++k) { rkn[k] = tok_row[tn * 4 + k] - rowbase; wkn[k] = ent_w[tn * 4 + k]; } } }
;         f32x4 v[4]; float s = 0.f;
; #pragma unroll
;         for (int j = 0; j < 4; ++j) {
;             f32x4 m = (f32x4){0.f, 0.f, 0.f, 0.f};
; #pragma unroll
;             for (int k = 0; k < 4; ++k) { const u32x2 o = ok[j][k]; m.x += wk[k] * bflo(o.x); m.y += wk[k] * bfhi(o.x); m.z += wk[k] * bflo(o.y); m.w += wk[k] * bfhi(o.y); }
;             v[j] = (f32x4){bflo(xw[j].x), bfhi(xw[j].x), bflo(xw[j].y), bfhi(xw[j].y)} + g2[64 * j] * m;
;             s += (v[j].x * v[j].x + v[j].y * v[j].y) + (v[j].z * v[j].z + v[j].w * v[j].w);
;         }
.LBB0_1239:
	s_ashr_i32 s9, s4, 13
	s_mul_i32 s26, s9, 0x1800
	s_ashr_i32 s27, s26, 31
	s_lshl_b64 s[26:27], s[26:27], 2
	s_add_u32 s26, s72, s26
	s_addc_u32 s27, s73, s27
	v_lshlrev_b32_e32 v10, 4, v252
	v_lshl_add_u64 v[74:75], s[26:27], 0, v[10:11]
	v_add_co_u32_e32 v70, vcc, s24, v74
	v_lshl_add_u64 v[78:79], v[74:75], 0, s[12:13]
	s_nop 0
	v_addc_co_u32_e32 v71, vcc, 0, v75, vcc
	global_load_dwordx4 v[70:73], v[70:71], off
	s_waitcnt vmcnt(16)
	v_lshlrev_b32_e32 v80, 16, v54
	global_load_dwordx4 v[74:77], v[78:79], off offset:1024
	v_and_b32_e32 v81, 0xffff0000, v54
	v_lshlrev_b32_e32 v88, 16, v55
	v_and_b32_e32 v89, 0xffff0000, v55
	v_lshlrev_b32_e32 v90, 16, v52
	v_and_b32_e32 v91, 0xffff0000, v52
	v_lshlrev_b32_e32 v92, 16, v53
	v_and_b32_e32 v93, 0xffff0000, v53
	global_load_dwordx4 v[52:55], v[78:79], off offset:2048
	s_waitcnt vmcnt(17)
	v_lshlrev_b32_e32 v94, 16, v44
	v_and_b32_e32 v95, 0xffff0000, v44
	v_lshlrev_b32_e32 v44, 16, v45
	v_and_b32_e32 v45, 0xffff0000, v45
	v_lshlrev_b32_e32 v102, 16, v42
	v_and_b32_e32 v103, 0xffff0000, v42
	v_lshlrev_b32_e32 v104, 16, v43
	v_and_b32_e32 v105, 0xffff0000, v43
	s_waitcnt vmcnt(16)
	v_lshlrev_b32_e32 v42, 16, v34
	v_and_b32_e32 v43, 0xffff0000, v34
	v_pk_fma_f32 v[108:109], v[6:7], v[44:45], 0 op_sel_hi:[0,1,0]
	v_pk_fma_f32 v[110:111], v[6:7], v[42:43], 0 op_sel_hi:[0,1,0]
	global_load_dwordx4 v[42:45], v[78:79], off offset:3072
	s_waitcnt vmcnt(15)
	v_lshlrev_b32_e32 v82, 16, v56
	v_and_b32_e32 v83, 0xffff0000, v56
	v_lshlrev_b32_e32 v56, 16, v57
	v_and_b32_e32 v57, 0xffff0000, v57
	s_waitcnt vmcnt(14)
	v_lshlrev_b32_e32 v96, 16, v46
	v_and_b32_e32 v97, 0xffff0000, v46
	v_lshlrev_b32_e32 v46, 16, v47
	v_and_b32_e32 v47, 0xffff0000, v47
	v_pk_fma_f32 v[80:81], v[6:7], v[80:81], 0 op_sel_hi:[0,1,0]
	v_pk_fma_f32 v[88:89], v[6:7], v[88:89], 0 op_sel_hi:[0,1,0]
	v_pk_fma_f32 v[94:95], v[6:7], v[94:95], 0 op_sel_hi:[0,1,0]
	s_waitcnt vmcnt(11)
	v_lshlrev_b32_e32 v84, 16, v58
	v_and_b32_e32 v85, 0xffff0000, v58
	v_lshlrev_b32_e32 v58, 16, v59
	v_and_b32_e32 v59, 0xffff0000, v59
	s_waitcnt vmcnt(10)
	v_lshlrev_b32_e32 v98, 16, v48
	v_and_b32_e32 v99, 0xffff0000, v48
	v_lshlrev_b32_e32 v48, 16, v49
	v_and_b32_e32 v49, 0xffff0000, v49
	v_pk_fma_f32 v[80:81], v[6:7], v[82:83], v[80:81] op_sel:[1,0,0]
	v_pk_fma_f32 v[56:57], v[6:7], v[56:57], v[88:89] op_sel:[1,0,0]
	v_pk_fma_f32 v[78:79], v[6:7], v[96:97], v[94:95] op_sel:[1,0,0]
	v_pk_fma_f32 v[46:47], v[6:7], v[46:47], v[108:109] op_sel:[1,0,0]
	s_waitcnt vmcnt(7)
	v_lshlrev_b32_e32 v86, 16, v60
	v_and_b32_e32 v87, 0xffff0000, v60
	v_lshlrev_b32_e32 v60, 16, v61
	v_and_b32_e32 v61, 0xffff0000, v61
	s_waitcnt vmcnt(6)
	v_lshlrev_b32_e32 v100, 16, v50
	v_and_b32_e32 v101, 0xffff0000, v50
	v_lshlrev_b32_e32 v50, 16, v51
	v_and_b32_e32 v51, 0xffff0000, v51
	v_pk_fma_f32 v[80:81], v[8:9], v[84:85], v[80:81] op_sel_hi:[0,1,1]
	v_pk_fma_f32 v[56:57], v[8:9], v[58:59], v[56:57] op_sel_hi:[0,1,1]
	v_pk_fma_f32 v[58:59], v[8:9], v[98:99], v[78:79] op_sel_hi:[0,1,1]
	v_pk_fma_f32 v[46:47], v[8:9], v[48:49], v[46:47] op_sel_hi:[0,1,1]
	v_pk_fma_f32 v[48:49], v[8:9], v[86:87], v[80:81] op_sel:[1,0,0]
	v_pk_fma_f32 v[56:57], v[8:9], v[60:61], v[56:57] op_sel:[1,0,0]
	v_pk_fma_f32 v[58:59], v[8:9], v[100:101], v[58:59] op_sel:[1,0,0]
	v_pk_fma_f32 v[46:47], v[8:9], v[50:51], v[46:47] op_sel:[1,0,0]
	v_lshlrev_b32_e32 v34, 16, v35
	v_and_b32_e32 v35, 0xffff0000, v35
	v_lshlrev_b32_e32 v106, 16, v36
	v_and_b32_e32 v107, 0xffff0000, v36
	v_pk_fma_f32 v[34:35], v[6:7], v[34:35], 0 op_sel_hi:[0,1,0]
	v_lshlrev_b32_e32 v36, 16, v37
	v_and_b32_e32 v37, 0xffff0000, v37
	v_pk_fma_f32 v[34:35], v[6:7], v[36:37], v[34:35] op_sel:[1,0,0]
	v_lshlrev_b32_e32 v36, 16, v39
	v_and_b32_e32 v37, 0xffff0000, v39
	v_pk_fma_f32 v[34:35], v[8:9], v[36:37], v[34:35] op_sel_hi:[0,1,1]
	s_waitcnt vmcnt(5)
	v_lshlrev_b32_e32 v36, 16, v41
	v_and_b32_e32 v37, 0xffff0000, v41
	v_pk_fma_f32 v[34:35], v[8:9], v[36:37], v[34:35] op_sel:[1,0,0]
	v_lshlrev_b32_e32 v36, 16, v32
	v_and_b32_e32 v37, 0xffff0000, v32
	v_lshlrev_b32_e32 v32, 16, v33
	s_waitcnt vmcnt(3)
	v_pk_fma_f32 v[50:51], v[56:57], v[72:73], v[92:93]
	v_pk_fma_f32 v[48:49], v[48:49], v[70:71], v[90:91]
	s_waitcnt vmcnt(2)
	v_pk_fma_f32 v[46:47], v[46:47], v[76:77], v[104:105]
	v_pk_fma_f32 v[56:57], v[58:59], v[74:75], v[102:103]
	v_pk_mul_f32 v[58:59], v[48:49], v[48:49]
	v_pk_mul_f32 v[60:61], v[50:51], v[50:51]
	v_pk_mul_f32 v[70:71], v[46:47], v[46:47]
	v_pk_mul_f32 v[72:73], v[56:57], v[56:57]
	v_pk_mov_b32 v[74:75], v[58:59], v[60:61] op_sel:[1,0]
	v_mov_b32_e32 v59, v61
	v_pk_mov_b32 v[60:61], v[72:73], v[70:71] op_sel:[1,0]
	v_mov_b32_e32 v73, v71
	v_pk_add_f32 v[60:61], v[60:61], v[72:73]
	v_pk_fma_f32 v[70:71], v[6:7], v[106:107], v[110:111] op_sel:[1,0,0]
	v_lshlrev_b32_e32 v72, 16, v38
	v_and_b32_e32 v73, 0xffff0000, v38
	v_pk_fma_f32 v[70:71], v[8:9], v[72:73], v[70:71] op_sel_hi:[0,1,1]
	v_lshlrev_b32_e32 v72, 16, v40
	v_and_b32_e32 v73, 0xffff0000, v40
	v_pk_fma_f32 v[70:71], v[8:9], v[72:73], v[70:71] op_sel:[1,0,0]
	v_and_b32_e32 v33, 0xffff0000, v33
	s_waitcnt vmcnt(1)
; __device__ __forceinline__ float wave_sum(float v) {
; #pragma unroll
;     for (int o = 1; o < 64; o <<= 1) v += __shfl_xor(v, o);
;     return v;
; __device__ __forceinline__ void p_final(const Args& a, const Frame& F, int half) {
;     ...
;             s += (v[j].x * v[j].x + v[j].y * v[j].y) + (v[j].z * v[j].z + v[j].w * v[j].w);
;         }
;         const float rstd = rsqrtf(wave_sum(s) * (1.f / D) + EPS);
; #pragma unroll
;         for (int j = 0; j < 4; ++j) xr[64 * j] = v[j] * rstd * fw[64 * j];
	v_pk_fma_f32 v[32:33], v[34:35], v[54:55], v[32:33]
	v_pk_fma_f32 v[34:35], v[70:71], v[52:53], v[36:37]
	v_lshlrev_b32_e32 v36, 16, v28
	v_and_b32_e32 v37, 0xffff0000, v28
	v_pk_fma_f32 v[36:37], v[6:7], v[36:37], 0 op_sel_hi:[0,1,0]
	v_lshlrev_b32_e32 v38, 16, v30
	v_and_b32_e32 v39, 0xffff0000, v30
	v_pk_fma_f32 v[36:37], v[6:7], v[38:39], v[36:37] op_sel:[1,0,0]
	v_lshlrev_b32_e32 v38, 16, v24
	v_and_b32_e32 v39, 0xffff0000, v24
	v_pk_fma_f32 v[36:37], v[8:9], v[38:39], v[36:37] op_sel_hi:[0,1,1]
	v_lshlrev_b32_e32 v38, 16, v26
	v_and_b32_e32 v39, 0xffff0000, v26
	v_lshlrev_b32_e32 v28, 16, v29
	v_and_b32_e32 v29, 0xffff0000, v29
	v_pk_fma_f32 v[36:37], v[8:9], v[38:39], v[36:37] op_sel:[1,0,0]
	v_pk_fma_f32 v[38:39], v[6:7], v[28:29], 0 op_sel_hi:[0,1,0]
	v_lshlrev_b32_e32 v40, 16, v31
	v_and_b32_e32 v41, 0xffff0000, v31
	v_pk_fma_f32 v[6:7], v[6:7], v[40:41], v[38:39] op_sel:[1,0,0]
	v_lshlrev_b32_e32 v24, 16, v25
	v_and_b32_e32 v25, 0xffff0000, v25
	v_pk_fma_f32 v[6:7], v[8:9], v[24:25], v[6:7] op_sel_hi:[0,1,1]
	v_lshlrev_b32_e32 v24, 16, v27
	v_and_b32_e32 v25, 0xffff0000, v27
	v_pk_fma_f32 v[6:7], v[8:9], v[24:25], v[6:7] op_sel:[1,0,0]
	v_lshlrev_b32_e32 v8, 16, v22
	v_and_b32_e32 v9, 0xffff0000, v22
	v_pk_add_f32 v[58:59], v[74:75], v[58:59]
	v_lshlrev_b32_e32 v22, 16, v23
	v_and_b32_e32 v23, 0xffff0000, v23
	s_waitcnt vmcnt(0)
	v_pk_fma_f32 v[36:37], v[36:37], v[42:43], v[8:9]
	v_pk_fma_f32 v[26:27], v[6:7], v[44:45], v[22:23]
	v_mul_f32_e32 v8, v36, v36
	v_pk_add_f32 v[6:7], v[58:59], v[58:59] op_sel:[0,1] op_sel_hi:[1,0]
	v_mul_f32_e32 v10, v37, v37
	v_mov_b32_e32 v7, v8
	v_pk_add_f32 v[8:9], v[60:61], v[60:61] op_sel:[0,1] op_sel_hi:[1,0]
	v_mul_f32_e32 v22, v26, v26
	v_mov_b32_e32 v9, v10
	v_pk_add_f32 v[6:7], v[6:7], v[8:9]
	v_mul_f32_e32 v8, v35, v35
	v_pk_fma_f32 v[8:9], v[34:35], v[34:35], v[8:9] op_sel_hi:[1,1,0]
	v_mul_f32_e32 v10, v33, v33
	v_mul_f32_e32 v24, v27, v27
	v_mov_b32_e32 v9, v22
	v_pk_fma_f32 v[22:23], v[32:33], v[32:33], v[10:11] op_sel_hi:[1,1,0]
	s_add_u32 s4, s4, s6
	v_mov_b32_e32 v23, v24
	v_pk_add_f32 v[8:9], v[8:9], v[22:23]
	s_addc_u32 s5, s5, s7
	v_pk_add_f32 v[6:7], v[6:7], v[8:9]
	s_add_i32 s8, s8, s23
	v_add_f32_e32 v6, v6, v7
	s_cmp_lt_i32 s4, s14
	s_nop 1
	v_add_f32_dpp v6, v6, v6 row_ror:8 row_mask:0xf bank_mask:0xf bound_ctrl:1
	s_nop 1
	v_add_f32_dpp v6, v6, v6 row_ror:4 row_mask:0xf bank_mask:0xf bound_ctrl:1
	s_nop 1
	v_add_f32_dpp v6, v6, v6 row_ror:2 row_mask:0xf bank_mask:0xf bound_ctrl:1
	s_nop 1
	v_add_f32_dpp v6, v6, v6 row_ror:1 row_mask:0xf bank_mask:0xf bound_ctrl:1
	s_nop 1
	v_mov_b32_e32 v7, v6
	s_nop 1
	v_permlane16_swap_b32_e32 v6, v7
	s_nop 1
	v_add_f32_e32 v6, v6, v7
	v_mov_b32_e32 v7, v6
	s_nop 1
	v_permlane32_swap_b32_e32 v6, v7
	s_nop 1
	v_add_f32_e32 v6, v6, v7
	v_fmamk_f32 v6, v6, 0x3a800000, v68
	v_mul_f32_e32 v7, 0x4b800000, v6
	v_cmp_gt_f32_e32 vcc, s25, v6
	s_nop 1
	v_cndmask_b32_e32 v6, v6, v7, vcc
	v_rsq_f32_e32 v6, v6
	s_nop 0
	v_mul_f32_e32 v7, 0x45800000, v6
	v_cndmask_b32_e32 v10, v6, v7, vcc
	v_pk_mul_f32 v[6:7], v[48:49], v[10:11] op_sel_hi:[1,0]
	v_pk_mul_f32 v[8:9], v[50:51], v[10:11] op_sel_hi:[1,0]
	s_waitcnt vmcnt(0)
	v_pk_mul_f32 v[6:7], v[120:121], v[6:7]
	v_pk_mul_f32 v[8:9], v[122:123], v[8:9]
	global_store_dwordx4 v[16:17], v[6:9], off offset:-3072
	v_pk_mul_f32 v[22:23], v[46:47], v[10:11] op_sel_hi:[1,0]
	v_pk_mul_f32 v[24:25], v[56:57], v[10:11] op_sel_hi:[1,0]
	v_pk_mul_f32 v[8:9], v[126:127], v[22:23]
	v_pk_mul_f32 v[6:7], v[124:125], v[24:25]
	global_store_dwordx4 v[16:17], v[6:9], off offset:-2048
	v_pk_mul_f32 v[22:23], v[32:33], v[10:11] op_sel_hi:[1,0]
	v_pk_mul_f32 v[24:25], v[34:35], v[10:11] op_sel_hi:[1,0]
	v_pk_mul_f32 v[8:9], v[130:131], v[22:23]
	v_pk_mul_f32 v[6:7], v[128:129], v[24:25]
	global_store_dwordx4 v[16:17], v[6:9], off offset:-1024
	s_nop 1
	v_mov_b64_e32 v[6:7], v[20:21]
	v_pk_mul_f32 v[8:9], v[26:27], v[10:11] op_sel_hi:[1,0]
	v_pk_mul_f32 v[20:21], v[36:37], v[10:11] op_sel_hi:[1,0]
	v_pk_mul_f32 v[20:21], v[132:133], v[20:21]
	v_pk_mul_f32 v[22:23], v[134:135], v[8:9]
	global_store_dwordx4 v[16:17], v[20:23], off
	v_lshl_add_u64 v[16:17], v[16:17], 0, s[10:11]
	v_mov_b64_e32 v[8:9], v[18:19]
	s_cbranch_scc0 .LBB0_1242

; __device__ __forceinline__ float bflo(unsigned w) { return __uint_as_float(w << 16); }
; __device__ __forceinline__ float bfhi(unsigned w) { return __uint_as_float(w & 0xffff0000u); }
; __device__ __forceinline__ void p_final(const Args& a, const Frame& F, int half) {
;     ...
;     for (int t = tbeg + gw; t < tend; t += NGW) {
;         f32x4* xr = (f32x4*)(a.out + (size_t)t * D) + F.lane;
;         const u32x2* x1p = (const u32x2*)x1_row(a.out, a.ws, t) + F.lane;
;         const f32x4* g2 = (const f32x4*)(mod + (t >> 13) * 6144 + 5120) + F.lane;
;         int rk[4]; float wk[4];
; #pragma unroll
;         for (int k = 0; k < 4; ++k) { rk[k] = rkn[k]; wk[k] = wkn[k]; }
;         u32x2 ok[4][4], xw[4];
; #pragma unroll
;         for (int j = 0; j < 4; ++j) { xw[j] = x1p[64 * j];
; #pragma unroll
;             for (int k = 0; k < 4; ++k) ok[j][k] = *((const u32x2*)(OUTK + (size_t)rk[k] * D) + F.lane + 64 * j); }
;         { const int tn = t + NGW; if (tn < tend) {
; #pragma unroll
;             for (int k = 0; k < 4; ++k) { rkn[k] = tok_row[tn * 4 + k] - rowbase; wkn[k] = ent_w[tn * 4 + k]; } } }
;         f32x4 v[4]; float s = 0.f;
; #pragma unroll
;         for (int j = 0; j < 4; ++j) {
;             f32x4 m = (f32x4){0.f, 0.f, 0.f, 0.f};
; #pragma unroll
;             for (int k = 0; k < 4; ++k) { const u32x2 o = ok[j][k]; m.x += wk[k] * bflo(o.x); m.y += wk[k] * bfhi(o.x); m.z += wk[k] * bflo(o.y); m.w += wk[k] * bfhi(o.y); }
;             v[j] = (f32x4){bflo(xw[j].x), bfhi(xw[j].x), bflo(xw[j].y), bfhi(xw[j].y)} + g2[64 * j] * m;
;             s += (v[j].x * v[j].x + v[j].y * v[j].y) + (v[j].z * v[j].z + v[j].w * v[j].w);
;         }
.LBB0_1395:
	s_ashr_i32 s7, s0, 13
	s_mul_i32 s22, s7, 0x1800
	s_ashr_i32 s23, s22, 31
	s_lshl_b64 s[22:23], s[22:23], 2
	s_add_u32 s22, s72, s22
	s_addc_u32 s23, s73, s23
	v_lshlrev_b32_e32 v4, 4, v252
	v_lshl_add_u64 v[74:75], s[22:23], 0, v[4:5]
	v_add_co_u32_e32 v70, vcc, s14, v74
	v_lshl_add_u64 v[78:79], v[74:75], 0, s[4:5]
	s_nop 0
	v_addc_co_u32_e32 v71, vcc, 0, v75, vcc
	global_load_dwordx4 v[70:73], v[70:71], off
	s_waitcnt vmcnt(16)
	v_lshlrev_b32_e32 v80, 16, v52
	global_load_dwordx4 v[74:77], v[78:79], off offset:1024
	v_and_b32_e32 v81, 0xffff0000, v52
	v_lshlrev_b32_e32 v88, 16, v53
	v_and_b32_e32 v89, 0xffff0000, v53
	v_lshlrev_b32_e32 v90, 16, v50
	v_and_b32_e32 v91, 0xffff0000, v50
	v_lshlrev_b32_e32 v92, 16, v51
	v_and_b32_e32 v93, 0xffff0000, v51
	global_load_dwordx4 v[50:53], v[78:79], off offset:2048
	s_waitcnt vmcnt(17)
	v_lshlrev_b32_e32 v94, 16, v42
	v_and_b32_e32 v95, 0xffff0000, v42
	v_lshlrev_b32_e32 v42, 16, v43
	v_and_b32_e32 v43, 0xffff0000, v43
	v_lshlrev_b32_e32 v102, 16, v40
	v_and_b32_e32 v103, 0xffff0000, v40
	v_lshlrev_b32_e32 v104, 16, v41
	v_and_b32_e32 v105, 0xffff0000, v41
	s_waitcnt vmcnt(16)
	v_lshlrev_b32_e32 v40, 16, v32
	v_and_b32_e32 v41, 0xffff0000, v32
	v_pk_fma_f32 v[108:109], v[0:1], v[42:43], 0 op_sel_hi:[0,1,0]
	v_pk_fma_f32 v[110:111], v[0:1], v[40:41], 0 op_sel_hi:[0,1,0]
	global_load_dwordx4 v[40:43], v[78:79], off offset:3072
	s_waitcnt vmcnt(15)
	v_lshlrev_b32_e32 v82, 16, v54
	v_and_b32_e32 v83, 0xffff0000, v54
	v_lshlrev_b32_e32 v54, 16, v55
	v_and_b32_e32 v55, 0xffff0000, v55
	s_waitcnt vmcnt(14)
	v_lshlrev_b32_e32 v96, 16, v44
	v_and_b32_e32 v97, 0xffff0000, v44
	v_lshlrev_b32_e32 v44, 16, v45
	v_and_b32_e32 v45, 0xffff0000, v45
	v_pk_fma_f32 v[80:81], v[0:1], v[80:81], 0 op_sel_hi:[0,1,0]
	v_pk_fma_f32 v[88:89], v[0:1], v[88:89], 0 op_sel_hi:[0,1,0]
	v_pk_fma_f32 v[94:95], v[0:1], v[94:95], 0 op_sel_hi:[0,1,0]
	s_waitcnt vmcnt(11)
	v_lshlrev_b32_e32 v84, 16, v56
	v_and_b32_e32 v85, 0xffff0000, v56
	v_lshlrev_b32_e32 v56, 16, v57
	v_and_b32_e32 v57, 0xffff0000, v57
	s_waitcnt vmcnt(10)
	v_lshlrev_b32_e32 v98, 16, v46
	v_and_b32_e32 v99, 0xffff0000, v46
	v_lshlrev_b32_e32 v46, 16, v47
	v_and_b32_e32 v47, 0xffff0000, v47
	v_pk_fma_f32 v[80:81], v[0:1], v[82:83], v[80:81] op_sel:[1,0,0]
	v_pk_fma_f32 v[54:55], v[0:1], v[54:55], v[88:89] op_sel:[1,0,0]
	v_pk_fma_f32 v[78:79], v[0:1], v[96:97], v[94:95] op_sel:[1,0,0]
	v_pk_fma_f32 v[44:45], v[0:1], v[44:45], v[108:109] op_sel:[1,0,0]
	s_waitcnt vmcnt(7)
	v_lshlrev_b32_e32 v86, 16, v58
	v_and_b32_e32 v87, 0xffff0000, v58
	v_lshlrev_b32_e32 v58, 16, v59
	v_and_b32_e32 v59, 0xffff0000, v59
	s_waitcnt vmcnt(6)
	v_lshlrev_b32_e32 v100, 16, v48
	v_and_b32_e32 v101, 0xffff0000, v48
	v_lshlrev_b32_e32 v48, 16, v49
	v_and_b32_e32 v49, 0xffff0000, v49
	v_pk_fma_f32 v[80:81], v[2:3], v[84:85], v[80:81] op_sel_hi:[0,1,1]
	v_pk_fma_f32 v[54:55], v[2:3], v[56:57], v[54:55] op_sel_hi:[0,1,1]
	v_pk_fma_f32 v[56:57], v[2:3], v[98:99], v[78:79] op_sel_hi:[0,1,1]
	v_pk_fma_f32 v[44:45], v[2:3], v[46:47], v[44:45] op_sel_hi:[0,1,1]
	v_pk_fma_f32 v[46:47], v[2:3], v[86:87], v[80:81] op_sel:[1,0,0]
	v_pk_fma_f32 v[54:55], v[2:3], v[58:59], v[54:55] op_sel:[1,0,0]
	v_pk_fma_f32 v[56:57], v[2:3], v[100:101], v[56:57] op_sel:[1,0,0]
	v_pk_fma_f32 v[44:45], v[2:3], v[48:49], v[44:45] op_sel:[1,0,0]
	v_lshlrev_b32_e32 v32, 16, v33
	v_and_b32_e32 v33, 0xffff0000, v33
	v_lshlrev_b32_e32 v106, 16, v34
	v_and_b32_e32 v107, 0xffff0000, v34
	v_pk_fma_f32 v[32:33], v[0:1], v[32:33], 0 op_sel_hi:[0,1,0]
	v_lshlrev_b32_e32 v34, 16, v35
	v_and_b32_e32 v35, 0xffff0000, v35
	v_pk_fma_f32 v[32:33], v[0:1], v[34:35], v[32:33] op_sel:[1,0,0]
	v_lshlrev_b32_e32 v34, 16, v37
	v_and_b32_e32 v35, 0xffff0000, v37
	v_pk_fma_f32 v[32:33], v[2:3], v[34:35], v[32:33] op_sel_hi:[0,1,1]
	s_waitcnt vmcnt(5)
	v_lshlrev_b32_e32 v34, 16, v39
	v_and_b32_e32 v35, 0xffff0000, v39
	v_pk_fma_f32 v[32:33], v[2:3], v[34:35], v[32:33] op_sel:[1,0,0]
	v_lshlrev_b32_e32 v34, 16, v30
	v_and_b32_e32 v35, 0xffff0000, v30
	v_lshlrev_b32_e32 v30, 16, v31
	s_waitcnt vmcnt(3)
	v_pk_fma_f32 v[48:49], v[54:55], v[72:73], v[92:93]
	v_pk_fma_f32 v[46:47], v[46:47], v[70:71], v[90:91]
	s_waitcnt vmcnt(2)
; __device__ __forceinline__ float wave_sum(float v) {
; #pragma unroll
;     for (int o = 1; o < 64; o <<= 1) v += __shfl_xor(v, o);
;     return v;
; __device__ __forceinline__ void p_final(const Args& a, const Frame& F, int half) {
;     ...
;             s += (v[j].x * v[j].x + v[j].y * v[j].y) + (v[j].z * v[j].z + v[j].w * v[j].w);
;         }
;         const float rstd = rsqrtf(wave_sum(s) * (1.f / D) + EPS);
; #pragma unroll
;         for (int j = 0; j < 4; ++j) xr[64 * j] = v[j] * rstd * fw[64 * j];
	v_pk_fma_f32 v[44:45], v[44:45], v[76:77], v[104:105]
	v_pk_fma_f32 v[54:55], v[56:57], v[74:75], v[102:103]
	v_pk_mul_f32 v[56:57], v[46:47], v[46:47]
	v_pk_mul_f32 v[58:59], v[48:49], v[48:49]
	v_pk_mul_f32 v[70:71], v[44:45], v[44:45]
	v_pk_mul_f32 v[72:73], v[54:55], v[54:55]
	v_pk_mov_b32 v[74:75], v[56:57], v[58:59] op_sel:[1,0]
	v_mov_b32_e32 v57, v59
	v_pk_mov_b32 v[58:59], v[72:73], v[70:71] op_sel:[1,0]
	v_mov_b32_e32 v73, v71
	v_pk_add_f32 v[58:59], v[58:59], v[72:73]
	v_pk_fma_f32 v[70:71], v[0:1], v[106:107], v[110:111] op_sel:[1,0,0]
	v_lshlrev_b32_e32 v72, 16, v36
	v_and_b32_e32 v73, 0xffff0000, v36
	v_pk_fma_f32 v[70:71], v[2:3], v[72:73], v[70:71] op_sel_hi:[0,1,1]
	v_lshlrev_b32_e32 v72, 16, v38
	v_and_b32_e32 v73, 0xffff0000, v38
	v_pk_fma_f32 v[70:71], v[2:3], v[72:73], v[70:71] op_sel:[1,0,0]
	v_and_b32_e32 v31, 0xffff0000, v31
	s_waitcnt vmcnt(1)
	v_pk_fma_f32 v[30:31], v[32:33], v[52:53], v[30:31]
	v_pk_fma_f32 v[32:33], v[70:71], v[50:51], v[34:35]
	v_lshlrev_b32_e32 v34, 16, v26
	v_and_b32_e32 v35, 0xffff0000, v26
	v_pk_fma_f32 v[34:35], v[0:1], v[34:35], 0 op_sel_hi:[0,1,0]
	v_lshlrev_b32_e32 v36, 16, v28
	v_and_b32_e32 v37, 0xffff0000, v28
	v_pk_fma_f32 v[34:35], v[0:1], v[36:37], v[34:35] op_sel:[1,0,0]
	v_lshlrev_b32_e32 v36, 16, v22
	v_and_b32_e32 v37, 0xffff0000, v22
	v_pk_fma_f32 v[34:35], v[2:3], v[36:37], v[34:35] op_sel_hi:[0,1,1]
	v_lshlrev_b32_e32 v36, 16, v24
	v_and_b32_e32 v37, 0xffff0000, v24
	v_lshlrev_b32_e32 v26, 16, v27
	v_and_b32_e32 v27, 0xffff0000, v27
	v_pk_fma_f32 v[34:35], v[2:3], v[36:37], v[34:35] op_sel:[1,0,0]
	v_pk_fma_f32 v[36:37], v[0:1], v[26:27], 0 op_sel_hi:[0,1,0]
	v_lshlrev_b32_e32 v38, 16, v29
	v_and_b32_e32 v39, 0xffff0000, v29
	v_pk_fma_f32 v[0:1], v[0:1], v[38:39], v[36:37] op_sel:[1,0,0]
	v_lshlrev_b32_e32 v22, 16, v23
	v_and_b32_e32 v23, 0xffff0000, v23
	v_pk_fma_f32 v[0:1], v[2:3], v[22:23], v[0:1] op_sel_hi:[0,1,1]
	v_lshlrev_b32_e32 v22, 16, v25
	v_and_b32_e32 v23, 0xffff0000, v25
	v_pk_fma_f32 v[0:1], v[2:3], v[22:23], v[0:1] op_sel:[1,0,0]
	v_lshlrev_b32_e32 v2, 16, v20
	v_and_b32_e32 v3, 0xffff0000, v20
	v_pk_add_f32 v[56:57], v[74:75], v[56:57]
	v_lshlrev_b32_e32 v20, 16, v21
	v_and_b32_e32 v21, 0xffff0000, v21
	s_waitcnt vmcnt(0)
	v_pk_fma_f32 v[34:35], v[34:35], v[40:41], v[2:3]
	v_pk_fma_f32 v[24:25], v[0:1], v[42:43], v[20:21]
	v_mul_f32_e32 v2, v34, v34
	v_pk_add_f32 v[0:1], v[56:57], v[56:57] op_sel:[0,1] op_sel_hi:[1,0]
	v_mul_f32_e32 v4, v35, v35
	v_mov_b32_e32 v1, v2
	v_pk_add_f32 v[2:3], v[58:59], v[58:59] op_sel:[0,1] op_sel_hi:[1,0]
	v_mul_f32_e32 v20, v24, v24
	v_mov_b32_e32 v3, v4
	v_pk_add_f32 v[0:1], v[0:1], v[2:3]
	v_mul_f32_e32 v2, v33, v33
	v_pk_fma_f32 v[2:3], v[32:33], v[32:33], v[2:3] op_sel_hi:[1,1,0]
	v_mul_f32_e32 v4, v31, v31
	v_mul_f32_e32 v22, v25, v25
	v_mov_b32_e32 v3, v20
	v_pk_fma_f32 v[20:21], v[30:31], v[30:31], v[4:5] op_sel_hi:[1,1,0]
	s_add_u32 s0, s0, s2
	v_mov_b32_e32 v21, v22
	v_pk_add_f32 v[2:3], v[2:3], v[20:21]
	s_addc_u32 s1, s1, s3
	v_pk_add_f32 v[0:1], v[0:1], v[2:3]
	s_add_i32 s6, s6, s19
	v_add_f32_e32 v0, v0, v1
	s_cmp_lt_i32 s0, 0x10000
	s_nop 1
	v_add_f32_dpp v0, v0, v0 row_ror:8 row_mask:0xf bank_mask:0xf bound_ctrl:1
	s_nop 1
	v_add_f32_dpp v0, v0, v0 row_ror:4 row_mask:0xf bank_mask:0xf bound_ctrl:1
	s_nop 1
	v_add_f32_dpp v0, v0, v0 row_ror:2 row_mask:0xf bank_mask:0xf bound_ctrl:1
	s_nop 1
	v_add_f32_dpp v0, v0, v0 row_ror:1 row_mask:0xf bank_mask:0xf bound_ctrl:1
	s_nop 1
	v_mov_b32_e32 v1, v0
	s_nop 1
	v_permlane16_swap_b32_e32 v0, v1
	s_nop 1
	v_add_f32_e32 v0, v0, v1
	v_mov_b32_e32 v1, v0
	s_nop 1
	v_permlane32_swap_b32_e32 v0, v1
	s_nop 1
	v_add_f32_e32 v0, v0, v1
	v_fmamk_f32 v0, v0, 0x3a800000, v68
	v_mul_f32_e32 v1, 0x4b800000, v0
	v_cmp_gt_f32_e32 vcc, s20, v0
	s_nop 1
	v_cndmask_b32_e32 v0, v0, v1, vcc
	v_rsq_f32_e32 v0, v0
	s_nop 0
	v_mul_f32_e32 v1, 0x45800000, v0
	v_cndmask_b32_e32 v4, v0, v1, vcc
	v_pk_mul_f32 v[0:1], v[46:47], v[4:5] op_sel_hi:[1,0]
	v_pk_mul_f32 v[2:3], v[48:49], v[4:5] op_sel_hi:[1,0]
	s_waitcnt vmcnt(0)
	v_pk_mul_f32 v[0:1], v[120:121], v[0:1]
	v_pk_mul_f32 v[2:3], v[122:123], v[2:3]
	global_store_dwordx4 v[10:11], v[0:3], off offset:-3072
	v_pk_mul_f32 v[20:21], v[44:45], v[4:5] op_sel_hi:[1,0]
	v_pk_mul_f32 v[22:23], v[54:55], v[4:5] op_sel_hi:[1,0]
	v_pk_mul_f32 v[2:3], v[126:127], v[20:21]
	v_pk_mul_f32 v[0:1], v[124:125], v[22:23]
	global_store_dwordx4 v[10:11], v[0:3], off offset:-2048
	v_pk_mul_f32 v[20:21], v[30:31], v[4:5] op_sel_hi:[1,0]
	v_pk_mul_f32 v[22:23], v[32:33], v[4:5] op_sel_hi:[1,0]
	v_pk_mul_f32 v[2:3], v[130:131], v[20:21]
	v_pk_mul_f32 v[0:1], v[128:129], v[22:23]
	global_store_dwordx4 v[10:11], v[0:3], off offset:-1024
	s_nop 1
	v_mov_b64_e32 v[0:1], v[18:19]
	v_pk_mul_f32 v[2:3], v[24:25], v[4:5] op_sel_hi:[1,0]
	v_pk_mul_f32 v[18:19], v[34:35], v[4:5] op_sel_hi:[1,0]
	v_pk_mul_f32 v[18:19], v[132:133], v[18:19]
	v_pk_mul_f32 v[20:21], v[134:135], v[2:3]
	global_store_dwordx4 v[10:11], v[18:21], off
	v_lshl_add_u64 v[10:11], v[10:11], 0, s[8:9]
	v_mov_b64_e32 v[2:3], v[16:17]
	s_cbranch_scc0 .LBB0_1398
